# v38 + P5 SwiGLU epilogue instruction selection: merged constant multiplies, pk_add+pk_mul fused to pk_fma (108 fewer VALU ops per wave per unit)
# speedup vs baseline: 1.0017x; 1.0017x over previous
.LBB0_648:
	s_mov_b32 m0, s85
	ds_read_b64_tr_b16 v[198:199], v187
	ds_read_b64_tr_b16 v[180:181], v187 offset:32
	ds_read_b64_tr_b16 v[202:203], v187 offset:64
	ds_read_b64_tr_b16 v[176:177], v187 offset:96
	ds_read_b64_tr_b16 v[200:201], v188
	ds_read_b64_tr_b16 v[182:183], v188 offset:32
	ds_read_b64_tr_b16 v[204:205], v188 offset:64
	ds_read_b64_tr_b16 v[178:179], v188 offset:96
	ds_read_b128 v[206:209], v186
	ds_read_b128 v[210:213], v186 offset:2048
	ds_read_b128 v[214:217], v186 offset:4096
	buffer_load_dwordx4 v189, s[20:23], s49 offen lds
	s_mov_b32 m0, s7
	s_add_i32 s16, s65, -1
	buffer_load_dwordx4 v192, s[20:23], s49 offen lds
	s_mov_b32 m0, s6
	s_and_b32 s25, s67, 0xffff
	buffer_load_dwordx4 v191, s[20:23], s49 offen lds
	s_mov_b32 m0, s47
	s_mov_b32 s24, s66
	buffer_load_dwordx4 v190, s[20:23], s49 offen lds
	s_mov_b32 m0, s48
	s_mov_b32 s26, s18
	buffer_load_dwordx4 v193, s[20:23], s49 offen lds
	v_mbcnt_lo_u32_b32 v189, -1, 0
	v_mbcnt_hi_u32_b32 v189, -1, v189
	s_mov_b32 s27, s19
	v_ashrrev_i32_e32 v190, 2, v189
	v_add_u32_e32 v190, s78, v190
	v_add_u32_e32 v191, s81, v190
	v_min_i32_e32 v192, s16, v191
	v_add_u32_e32 v193, 64, v191
	v_add_u32_e32 v195, 0x80, v191
	v_add_u32_e32 v191, 0xc0, v191
	v_add_u32_e32 v190, s82, v190
	v_min_i32_e32 v193, s16, v193
	v_min_i32_e32 v195, s16, v195
	v_min_i32_e32 v191, s16, v191
	v_min_i32_e32 v190, s16, v190
	v_lshlrev_b32_e32 v192, 2, v192
	v_lshlrev_b32_e32 v193, 2, v193
	v_lshlrev_b32_e32 v195, 2, v195
	v_lshlrev_b32_e32 v191, 2, v191
	v_lshlrev_b32_e32 v190, 2, v190
	buffer_load_dword v192, v192, s[24:27], 0 offen
	s_nop 0
	buffer_load_dword v193, v193, s[24:27], 0 offen
	s_nop 0
	buffer_load_dword v195, v195, s[24:27], 0 offen
	s_nop 0
	buffer_load_dword v191, v191, s[24:27], 0 offen
	s_nop 0
	buffer_load_dword v190, v190, s[24:27], 0 offen
	v_lshlrev_b32_e32 v197, 4, v189
	v_and_b32_e32 v189, 32, v189
	v_and_b32_e32 v197, 48, v197
	v_bitop3_b32 v197, v197, s84, v189 bitop3:0xde
	s_and_b32 s25, s77, 0xffff
	s_mov_b32 s24, s55
	s_and_b32 s29, s80, 0xffff
	s_mov_b32 s28, s79
	s_mov_b32 s16, s55
	s_mov_b32 s36, s79
	s_mov_b32 s38, s18
	s_mov_b32 s39, s19
	s_waitcnt lgkmcnt(2)
	v_mfma_f32_16x16x32_bf16 v[172:175], v[198:201], v[206:209], v[172:175]
	s_mov_b32 s17, s25
	s_mov_b32 s37, s29
	s_waitcnt vmcnt(4)
	v_lshlrev_b32_e32 v189, 10, v192
	s_waitcnt vmcnt(3)
	v_lshlrev_b32_e32 v192, 10, v193
	s_waitcnt vmcnt(2)
	v_lshlrev_b32_e32 v193, 10, v195
	s_waitcnt vmcnt(1)
	v_lshlrev_b32_e32 v195, 10, v191
	s_waitcnt vmcnt(0)
	v_lshlrev_b32_e32 v218, 10, v190
	v_and_or_b32 v189, v189, s83, v197
	v_and_or_b32 v192, v192, s83, v197
	v_and_or_b32 v191, v193, s83, v197
	v_and_or_b32 v190, v195, s83, v197
	v_and_or_b32 v193, v218, s83, v197
	v_mfma_f32_16x16x32_bf16 v[168:171], v[180:183], v[206:209], v[168:171]
	v_mfma_f32_16x16x32_bf16 v[164:167], v[202:205], v[206:209], v[164:167]
	v_mfma_f32_16x16x32_bf16 v[160:163], v[176:179], v[206:209], v[160:163]
	ds_read_b128 v[206:209], v186 offset:6144
	v_cvt_pk_bf16_f32 v15, v14, v15
	v_cvt_pk_bf16_f32 v14, v12, v13
	s_waitcnt lgkmcnt(2)
	v_mfma_f32_16x16x32_bf16 v[156:159], v[198:201], v[210:213], v[156:159]
	ds_write_b64 v185, v[14:15] offset:34816
	v_mfma_f32_16x16x32_bf16 v[152:155], v[180:183], v[210:213], v[152:155]
	v_mfma_f32_16x16x32_bf16 v[148:151], v[202:205], v[210:213], v[148:151]
	v_mfma_f32_16x16x32_bf16 v[144:147], v[176:179], v[210:213], v[144:147]
	buffer_load_dwordx4 v[12:15], v184, s[16:19], 0 offen
	ds_read_b128 v[210:213], v186 offset:8192
	s_waitcnt lgkmcnt(3)
	v_mfma_f32_16x16x32_bf16 v[132:135], v[198:201], v[214:217], v[132:135]
	v_mfma_f32_16x16x32_bf16 v[124:127], v[180:183], v[214:217], v[124:127]
	v_mfma_f32_16x16x32_bf16 v[120:123], v[202:205], v[214:217], v[120:123]
	v_mfma_f32_16x16x32_bf16 v[140:143], v[176:179], v[214:217], v[140:143]
	ds_read_b128 v[214:217], v186 offset:10240
	v_cvt_pk_bf16_f32 v3, v2, v3
	v_cvt_pk_bf16_f32 v2, v0, v1
	s_waitcnt lgkmcnt(3)
	v_mfma_f32_16x16x32_bf16 v[136:139], v[198:201], v[206:209], v[136:139]
	ds_write_b64 v185, v[2:3] offset:43520
	v_mfma_f32_16x16x32_bf16 v[128:131], v[180:183], v[206:209], v[128:131]
	v_mfma_f32_16x16x32_bf16 v[116:119], v[202:205], v[206:209], v[116:119]
	v_mfma_f32_16x16x32_bf16 v[112:115], v[176:179], v[206:209], v[112:115]
	buffer_load_dwordx4 v[0:3], v184, s[16:19], s19 offen
	ds_read_b128 v[206:209], v186 offset:12288
	s_waitcnt lgkmcnt(3)
	v_mfma_f32_16x16x32_bf16 v[100:103], v[198:201], v[210:213], v[100:103]
	v_mfma_f32_16x16x32_bf16 v[92:95], v[180:183], v[210:213], v[92:95]
	v_mfma_f32_16x16x32_bf16 v[88:91], v[202:205], v[210:213], v[88:91]
	v_mfma_f32_16x16x32_bf16 v[108:111], v[176:179], v[210:213], v[108:111]
	ds_read_b128 v[210:213], v186 offset:14336
	v_cvt_pk_bf16_f32 v31, v30, v31
	v_cvt_pk_bf16_f32 v30, v28, v29
	s_waitcnt lgkmcnt(3)
	v_mfma_f32_16x16x32_bf16 v[104:107], v[198:201], v[214:217], v[104:107]
	ds_write_b64 v185, v[30:31] offset:52224
	v_mfma_f32_16x16x32_bf16 v[96:99], v[180:183], v[214:217], v[96:99]
	v_mfma_f32_16x16x32_bf16 v[84:87], v[202:205], v[214:217], v[84:87]
	v_mfma_f32_16x16x32_bf16 v[80:83], v[176:179], v[214:217], v[80:83]
	buffer_load_dwordx4 v[28:31], v184, s[16:19], s87 offen
	ds_read_b128 v[214:217], v186 offset:16384
	s_waitcnt lgkmcnt(3)
	v_mfma_f32_16x16x32_bf16 v[72:75], v[198:201], v[206:209], v[72:75]
	v_mfma_f32_16x16x32_bf16 v[64:67], v[180:183], v[206:209], v[64:67]
	v_mfma_f32_16x16x32_bf16 v[60:63], v[202:205], v[206:209], v[60:63]
	v_mfma_f32_16x16x32_bf16 v[76:79], v[176:179], v[206:209], v[76:79]
	ds_read_b128 v[206:209], v186 offset:1024
	v_cvt_pk_bf16_f32 v27, v26, v27
	v_cvt_pk_bf16_f32 v26, v24, v25
	s_waitcnt lgkmcnt(3)
	v_mfma_f32_16x16x32_bf16 v[68:71], v[198:201], v[210:213], v[68:71]
	ds_write_b64 v185, v[26:27] offset:60928
	v_mfma_f32_16x16x32_bf16 v[56:59], v[180:183], v[210:213], v[56:59]
	v_mfma_f32_16x16x32_bf16 v[52:55], v[202:205], v[210:213], v[52:55]
	v_mfma_f32_16x16x32_bf16 v[48:51], v[176:179], v[210:213], v[48:51]
	buffer_load_dwordx4 v[24:27], v184, s[16:19], s88 offen
	ds_read_b128 v[210:213], v186 offset:3072
	s_waitcnt lgkmcnt(3)
	v_mfma_f32_16x16x32_bf16 v[44:47], v[198:201], v[214:217], v[44:47]
	ds_read_b64_tr_b16 v[200:201], v188 offset:17408
	ds_read_b64_tr_b16 v[220:221], v188 offset:17440
	ds_read_b64_tr_b16 v[198:199], v187 offset:17408
	ds_read_b64_tr_b16 v[218:219], v187 offset:17440
	v_mfma_f32_16x16x32_bf16 v[40:43], v[180:183], v[214:217], v[40:43]
	ds_read_b64_tr_b16 v[180:181], v187 offset:17472
	ds_read_b64_tr_b16 v[182:183], v188 offset:17472
	v_mfma_f32_16x16x32_bf16 v[32:35], v[176:179], v[214:217], v[32:35]
	ds_read_b64_tr_b16 v[176:177], v187 offset:17504
	ds_read_b64_tr_b16 v[178:179], v188 offset:17504
	v_mfma_f32_16x16x32_bf16 v[36:39], v[202:205], v[214:217], v[36:39]
	ds_read_b128 v[202:205], v186 offset:5120
	v_cvt_pk_bf16_f32 v23, v22, v23
	v_cvt_pk_bf16_f32 v22, v20, v21
	s_waitcnt lgkmcnt(6)
	v_mfma_f32_16x16x32_bf16 v[172:175], v[198:201], v[206:209], v[172:175]
	ds_write_b64 v185, v[22:23] offset:34880
	s_waitcnt lgkmcnt(6)
	v_mfma_f32_16x16x32_bf16 v[168:171], v[218:221], v[206:209], v[168:171]
	s_waitcnt lgkmcnt(4)
	v_mfma_f32_16x16x32_bf16 v[164:167], v[180:183], v[206:209], v[164:167]
	s_waitcnt lgkmcnt(2)
	v_mfma_f32_16x16x32_bf16 v[160:163], v[176:179], v[206:209], v[160:163]
	buffer_load_dwordx4 v[20:23], v184, s[36:39], 0 offen
	ds_read_b128 v[206:209], v186 offset:7168
	v_mfma_f32_16x16x32_bf16 v[156:159], v[198:201], v[210:213], v[156:159]
	v_mfma_f32_16x16x32_bf16 v[152:155], v[218:221], v[210:213], v[152:155]
	v_mfma_f32_16x16x32_bf16 v[148:151], v[180:183], v[210:213], v[148:151]
	v_mfma_f32_16x16x32_bf16 v[144:147], v[176:179], v[210:213], v[144:147]
	ds_read_b128 v[210:213], v186 offset:9216
	v_cvt_pk_bf16_f32 v7, v6, v7
	v_cvt_pk_bf16_f32 v6, v4, v5
	s_waitcnt lgkmcnt(3)
	v_mfma_f32_16x16x32_bf16 v[132:135], v[198:201], v[202:205], v[132:135]
	ds_write_b64 v185, v[6:7] offset:43584
	v_mfma_f32_16x16x32_bf16 v[124:127], v[218:221], v[202:205], v[124:127]
	v_mfma_f32_16x16x32_bf16 v[120:123], v[180:183], v[202:205], v[120:123]
	v_mfma_f32_16x16x32_bf16 v[140:143], v[176:179], v[202:205], v[140:143]
	buffer_load_dwordx4 v[4:7], v184, s[36:39], s19 offen
	ds_read_b128 v[202:205], v186 offset:11264
	s_waitcnt lgkmcnt(3)
	v_mfma_f32_16x16x32_bf16 v[136:139], v[198:201], v[206:209], v[136:139]
	v_mfma_f32_16x16x32_bf16 v[128:131], v[218:221], v[206:209], v[128:131]
	v_mfma_f32_16x16x32_bf16 v[116:119], v[180:183], v[206:209], v[116:119]
	v_mfma_f32_16x16x32_bf16 v[112:115], v[176:179], v[206:209], v[112:115]
	ds_read_b128 v[206:209], v186 offset:13312
	v_cvt_pk_bf16_f32 v11, v10, v11
	v_cvt_pk_bf16_f32 v10, v8, v9
	s_waitcnt lgkmcnt(3)
	v_mfma_f32_16x16x32_bf16 v[100:103], v[198:201], v[210:213], v[100:103]
	ds_write_b64 v185, v[10:11] offset:52288
	v_mfma_f32_16x16x32_bf16 v[92:95], v[218:221], v[210:213], v[92:95]
	v_mfma_f32_16x16x32_bf16 v[88:91], v[180:183], v[210:213], v[88:91]
	v_mfma_f32_16x16x32_bf16 v[108:111], v[176:179], v[210:213], v[108:111]
	buffer_load_dwordx4 v[8:11], v184, s[36:39], s87 offen
	ds_read_b128 v[210:213], v186 offset:15360
	s_waitcnt lgkmcnt(3)
	v_mfma_f32_16x16x32_bf16 v[104:107], v[198:201], v[202:205], v[104:107]
	v_mfma_f32_16x16x32_bf16 v[96:99], v[218:221], v[202:205], v[96:99]
	v_mfma_f32_16x16x32_bf16 v[84:87], v[180:183], v[202:205], v[84:87]
	v_mfma_f32_16x16x32_bf16 v[80:83], v[176:179], v[202:205], v[80:83]
	ds_read_b128 v[202:205], v186 offset:17408
	v_cvt_pk_bf16_f32 v19, v18, v19
	v_cvt_pk_bf16_f32 v18, v16, v17
	s_waitcnt lgkmcnt(3)
	v_mfma_f32_16x16x32_bf16 v[72:75], v[198:201], v[206:209], v[72:75]
	ds_write_b64 v185, v[18:19] offset:60992
	v_mfma_f32_16x16x32_bf16 v[64:67], v[218:221], v[206:209], v[64:67]
	v_mfma_f32_16x16x32_bf16 v[60:63], v[180:183], v[206:209], v[60:63]
	v_mfma_f32_16x16x32_bf16 v[76:79], v[176:179], v[206:209], v[76:79]
	buffer_load_dwordx4 v[16:19], v184, s[36:39], s88 offen
	s_waitcnt lgkmcnt(2)
	v_mfma_f32_16x16x32_bf16 v[68:71], v[198:201], v[210:213], v[68:71]
	v_mfma_f32_16x16x32_bf16 v[56:59], v[218:221], v[210:213], v[56:59]
	v_mfma_f32_16x16x32_bf16 v[52:55], v[180:183], v[210:213], v[52:55]
	v_mfma_f32_16x16x32_bf16 v[48:51], v[176:179], v[210:213], v[48:51]
	s_waitcnt lgkmcnt(1)
	v_mfma_f32_16x16x32_bf16 v[44:47], v[198:201], v[202:205], v[44:47]
	v_mfma_f32_16x16x32_bf16 v[40:43], v[218:221], v[202:205], v[40:43]
	v_mfma_f32_16x16x32_bf16 v[36:39], v[180:183], v[202:205], v[36:39]
	v_mfma_f32_16x16x32_bf16 v[32:35], v[176:179], v[202:205], v[32:35]
	s_waitcnt vmcnt(8)
	s_mov_b32 m0, s46
	s_waitcnt lgkmcnt(0)
	s_barrier
	ds_read_b64_tr_b16 v[178:179], v188 offset:34816
	ds_read_b64_tr_b16 v[176:177], v187 offset:34816
	ds_read_b64_tr_b16 v[180:181], v187 offset:34848
	ds_read_b64_tr_b16 v[198:199], v187 offset:34880
	ds_read_b64_tr_b16 v[202:203], v187 offset:34912
	ds_read_b128 v[206:209], v186 offset:36864
	ds_read_b64_tr_b16 v[182:183], v188 offset:34848
	ds_read_b64_tr_b16 v[200:201], v188 offset:34880
	ds_read_b64_tr_b16 v[204:205], v188 offset:34912
	ds_read_b128 v[210:213], v186 offset:38912
	ds_read_b128 v[214:217], v186 offset:40960
	buffer_load_dwordx4 v189, s[20:23], 0 offen lds
	s_mov_b32 m0, s86
	s_waitcnt lgkmcnt(5)
	v_mfma_f32_16x16x32_bf16 v[172:175], v[176:179], v[206:209], v[172:175]
	buffer_load_dwordx4 v192, s[20:23], 0 offen lds
	s_mov_b32 m0, s89
	s_nop 0
	buffer_load_dwordx4 v191, s[20:23], 0 offen lds
	s_mov_b32 m0, s90
	s_waitcnt lgkmcnt(4)
	v_mfma_f32_16x16x32_bf16 v[168:171], v[180:183], v[206:209], v[168:171]
	buffer_load_dwordx4 v190, s[20:23], 0 offen lds
	s_mov_b32 m0, s91
	s_nop 0
	buffer_load_dwordx4 v193, s[20:23], 0 offen lds
	s_waitcnt lgkmcnt(3)
	v_mfma_f32_16x16x32_bf16 v[164:167], v[198:201], v[206:209], v[164:167]
	s_waitcnt lgkmcnt(2)
	v_mfma_f32_16x16x32_bf16 v[160:163], v[202:205], v[206:209], v[160:163]
	ds_read_b128 v[206:209], v186 offset:43008
	s_waitcnt vmcnt(12)
	v_cvt_pk_bf16_f32 v15, v14, v15
	v_cvt_pk_bf16_f32 v14, v12, v13
	s_waitcnt lgkmcnt(2)
	v_mfma_f32_16x16x32_bf16 v[156:159], v[176:179], v[210:213], v[156:159]
	ds_write_b64 v185, v[14:15]
	v_mfma_f32_16x16x32_bf16 v[152:155], v[180:183], v[210:213], v[152:155]
	v_mfma_f32_16x16x32_bf16 v[148:151], v[198:201], v[210:213], v[148:151]
	v_mfma_f32_16x16x32_bf16 v[144:147], v[202:205], v[210:213], v[144:147]
	buffer_load_dwordx4 v[12:15], v184, s[16:19], s93 offen
	ds_read_b128 v[210:213], v186 offset:45056
	s_waitcnt lgkmcnt(3)
	v_mfma_f32_16x16x32_bf16 v[132:135], v[176:179], v[214:217], v[132:135]
	v_mfma_f32_16x16x32_bf16 v[124:127], v[180:183], v[214:217], v[124:127]
	v_mfma_f32_16x16x32_bf16 v[120:123], v[198:201], v[214:217], v[120:123]
	v_mfma_f32_16x16x32_bf16 v[140:143], v[202:205], v[214:217], v[140:143]
	ds_read_b128 v[214:217], v186 offset:47104
	s_waitcnt vmcnt(12)
	v_cvt_pk_bf16_f32 v3, v2, v3
	v_cvt_pk_bf16_f32 v2, v0, v1
	s_waitcnt lgkmcnt(3)
	v_mfma_f32_16x16x32_bf16 v[136:139], v[176:179], v[206:209], v[136:139]
	ds_write_b64 v185, v[2:3] offset:8704
	v_mfma_f32_16x16x32_bf16 v[128:131], v[180:183], v[206:209], v[128:131]
	v_mfma_f32_16x16x32_bf16 v[116:119], v[198:201], v[206:209], v[116:119]
	v_mfma_f32_16x16x32_bf16 v[112:115], v[202:205], v[206:209], v[112:115]
	buffer_load_dwordx4 v[0:3], v184, s[16:19], s94 offen
	ds_read_b128 v[206:209], v186 offset:49152
	s_waitcnt lgkmcnt(3)
	v_mfma_f32_16x16x32_bf16 v[100:103], v[176:179], v[210:213], v[100:103]
	v_mfma_f32_16x16x32_bf16 v[92:95], v[180:183], v[210:213], v[92:95]
	v_mfma_f32_16x16x32_bf16 v[88:91], v[198:201], v[210:213], v[88:91]
	v_mfma_f32_16x16x32_bf16 v[108:111], v[202:205], v[210:213], v[108:111]
	ds_read_b128 v[210:213], v186 offset:51200
	s_waitcnt vmcnt(12)
	v_cvt_pk_bf16_f32 v31, v30, v31
	v_cvt_pk_bf16_f32 v30, v28, v29
	s_waitcnt lgkmcnt(3)
	v_mfma_f32_16x16x32_bf16 v[104:107], v[176:179], v[214:217], v[104:107]
	ds_write_b64 v185, v[30:31] offset:17408
	v_mfma_f32_16x16x32_bf16 v[96:99], v[180:183], v[214:217], v[96:99]
	v_mfma_f32_16x16x32_bf16 v[84:87], v[198:201], v[214:217], v[84:87]
	v_mfma_f32_16x16x32_bf16 v[80:83], v[202:205], v[214:217], v[80:83]
	buffer_load_dwordx4 v[28:31], v184, s[16:19], s95 offen
	ds_read_b128 v[214:217], v186 offset:53248
	s_waitcnt lgkmcnt(3)
	v_mfma_f32_16x16x32_bf16 v[72:75], v[176:179], v[206:209], v[72:75]
	v_mfma_f32_16x16x32_bf16 v[64:67], v[180:183], v[206:209], v[64:67]
	v_mfma_f32_16x16x32_bf16 v[60:63], v[198:201], v[206:209], v[60:63]
	v_mfma_f32_16x16x32_bf16 v[76:79], v[202:205], v[206:209], v[76:79]
	ds_read_b128 v[206:209], v186 offset:37888
	s_waitcnt vmcnt(12)
	v_cvt_pk_bf16_f32 v27, v26, v27
	v_cvt_pk_bf16_f32 v26, v24, v25
	s_waitcnt lgkmcnt(3)
	v_mfma_f32_16x16x32_bf16 v[68:71], v[176:179], v[210:213], v[68:71]
	ds_write_b64 v185, v[26:27] offset:26112
	v_mfma_f32_16x16x32_bf16 v[56:59], v[180:183], v[210:213], v[56:59]
	v_mfma_f32_16x16x32_bf16 v[52:55], v[198:201], v[210:213], v[52:55]
	v_mfma_f32_16x16x32_bf16 v[48:51], v[202:205], v[210:213], v[48:51]
	buffer_load_dwordx4 v[24:27], v184, s[16:19], s96 offen
	ds_read_b128 v[210:213], v186 offset:39936
	s_waitcnt lgkmcnt(3)
	v_mfma_f32_16x16x32_bf16 v[44:47], v[176:179], v[214:217], v[44:47]
	ds_read_b64_tr_b16 v[178:179], v188 offset:52224
	ds_read_b64_tr_b16 v[220:221], v188 offset:52256
	ds_read_b64_tr_b16 v[176:177], v187 offset:52224
	ds_read_b64_tr_b16 v[218:219], v187 offset:52256
	v_mfma_f32_16x16x32_bf16 v[40:43], v[180:183], v[214:217], v[40:43]
	v_mfma_f32_16x16x32_bf16 v[180:183], v[198:201], v[214:217], v[36:39]
	ds_read_b64_tr_b16 v[198:199], v187 offset:52288
	ds_read_b64_tr_b16 v[200:201], v188 offset:52288
	v_mfma_f32_16x16x32_bf16 v[32:35], v[202:205], v[214:217], v[32:35]
	ds_read_b64_tr_b16 v[202:203], v187 offset:52320
	ds_read_b64_tr_b16 v[204:205], v188 offset:52320
	ds_read_b128 v[36:39], v186 offset:41984
	s_waitcnt vmcnt(12)
	v_cvt_pk_bf16_f32 v23, v22, v23
	v_cvt_pk_bf16_f32 v22, v20, v21
	s_waitcnt lgkmcnt(6)
	v_mfma_f32_16x16x32_bf16 v[214:217], v[176:179], v[206:209], v[172:175]
	ds_write_b64 v185, v[22:23] offset:64
	s_waitcnt lgkmcnt(6)
	v_mfma_f32_16x16x32_bf16 v[222:225], v[218:221], v[206:209], v[168:171]
	s_waitcnt lgkmcnt(4)
	v_mfma_f32_16x16x32_bf16 v[226:229], v[198:201], v[206:209], v[164:167]
	s_waitcnt lgkmcnt(2)
	v_mfma_f32_16x16x32_bf16 v[206:209], v[202:205], v[206:209], v[160:163]
	buffer_load_dwordx4 v[20:23], v184, s[36:39], s93 offen
	ds_read_b128 v[230:233], v186 offset:44032
	v_mfma_f32_16x16x32_bf16 v[172:175], v[176:179], v[210:213], v[156:159]
	v_mfma_f32_16x16x32_bf16 v[164:167], v[218:221], v[210:213], v[152:155]
	v_mfma_f32_16x16x32_bf16 v[168:171], v[198:201], v[210:213], v[148:151]
	v_mfma_f32_16x16x32_bf16 v[160:163], v[202:205], v[210:213], v[144:147]
	ds_read_b128 v[210:213], v186 offset:46080
	s_waitcnt vmcnt(12)
	v_cvt_pk_bf16_f32 v7, v6, v7
	v_cvt_pk_bf16_f32 v6, v4, v5
	s_waitcnt lgkmcnt(3)
	v_mfma_f32_16x16x32_bf16 v[156:159], v[176:179], v[36:39], v[132:135]
	ds_write_b64 v185, v[6:7] offset:8768
	v_mfma_f32_16x16x32_bf16 v[144:147], v[218:221], v[36:39], v[124:127]
	v_mfma_f32_16x16x32_bf16 v[152:155], v[198:201], v[36:39], v[120:123]
	v_mfma_f32_16x16x32_bf16 v[148:151], v[202:205], v[36:39], v[140:143]
	buffer_load_dwordx4 v[4:7], v184, s[36:39], s94 offen
	ds_read_b128 v[36:39], v186 offset:48128
	s_waitcnt lgkmcnt(3)
	v_mfma_f32_16x16x32_bf16 v[140:143], v[176:179], v[230:233], v[136:139]
	v_mfma_f32_16x16x32_bf16 v[132:135], v[218:221], v[230:233], v[128:131]
	v_mfma_f32_16x16x32_bf16 v[136:139], v[198:201], v[230:233], v[116:119]
	v_mfma_f32_16x16x32_bf16 v[128:131], v[202:205], v[230:233], v[112:115]
	ds_read_b128 v[230:233], v186 offset:50176
	s_waitcnt vmcnt(12)
	v_cvt_pk_bf16_f32 v11, v10, v11
	v_cvt_pk_bf16_f32 v10, v8, v9
	s_waitcnt lgkmcnt(3)
	v_mfma_f32_16x16x32_bf16 v[124:127], v[176:179], v[210:213], v[100:103]
	ds_write_b64 v185, v[10:11] offset:17472
	v_mfma_f32_16x16x32_bf16 v[112:115], v[218:221], v[210:213], v[92:95]
	v_mfma_f32_16x16x32_bf16 v[120:123], v[198:201], v[210:213], v[88:91]
	v_mfma_f32_16x16x32_bf16 v[116:119], v[202:205], v[210:213], v[108:111]
	buffer_load_dwordx4 v[8:11], v184, s[36:39], s95 offen
	ds_read_b128 v[210:213], v186 offset:52224
	s_waitcnt lgkmcnt(3)
	v_mfma_f32_16x16x32_bf16 v[108:111], v[176:179], v[36:39], v[104:107]
	v_mfma_f32_16x16x32_bf16 v[100:103], v[218:221], v[36:39], v[96:99]
	v_mfma_f32_16x16x32_bf16 v[104:107], v[198:201], v[36:39], v[84:87]
	v_mfma_f32_16x16x32_bf16 v[96:99], v[202:205], v[36:39], v[80:83]
	ds_read_b128 v[234:237], v186 offset:54272
	s_waitcnt vmcnt(12)
	v_cvt_pk_bf16_f32 v19, v18, v19
	v_cvt_pk_bf16_f32 v18, v16, v17
	s_waitcnt lgkmcnt(3)
	v_mfma_f32_16x16x32_bf16 v[92:95], v[176:179], v[230:233], v[72:75]
	ds_write_b64 v185, v[18:19] offset:26176
	v_mfma_f32_16x16x32_bf16 v[80:83], v[218:221], v[230:233], v[64:67]
	v_mfma_f32_16x16x32_bf16 v[88:91], v[198:201], v[230:233], v[60:63]
	v_mfma_f32_16x16x32_bf16 v[84:87], v[202:205], v[230:233], v[76:79]
	buffer_load_dwordx4 v[16:19], v184, s[36:39], s96 offen
	s_waitcnt lgkmcnt(2)
	v_mfma_f32_16x16x32_bf16 v[76:79], v[176:179], v[210:213], v[68:71]
	v_mfma_f32_16x16x32_bf16 v[68:71], v[218:221], v[210:213], v[56:59]
	v_mfma_f32_16x16x32_bf16 v[72:75], v[198:201], v[210:213], v[52:55]
	v_mfma_f32_16x16x32_bf16 v[64:67], v[202:205], v[210:213], v[48:51]
	s_waitcnt lgkmcnt(1)
	v_mfma_f32_16x16x32_bf16 v[52:55], v[176:179], v[234:237], v[44:47]
	v_mfma_f32_16x16x32_bf16 v[36:39], v[218:221], v[234:237], v[40:43]
	v_mfma_f32_16x16x32_bf16 v[48:51], v[198:201], v[234:237], v[180:183]
	v_mfma_f32_16x16x32_bf16 v[32:35], v[202:205], v[234:237], v[32:35]
	s_waitcnt vmcnt(8)
	s_waitcnt lgkmcnt(0)
	s_barrier
	v_mbcnt_lo_u32_b32 v178, -1, 0
	v_mbcnt_hi_u32_b32 v178, -1, v178
	s_add_i32 s16, s54, s4
	v_ashrrev_i32_e32 v40, 1, v178
	v_and_b32_e32 v40, -8, v40
	v_add_u32_e32 v176, s16, v40
	v_ashrrev_i32_e32 v177, 31, v176
	v_lshlrev_b64 v[40:41], 2, v[176:177]
	v_lshl_add_u64 v[42:43], s[56:57], 0, v[40:41]
	v_lshl_add_u64 v[40:41], s[58:59], 0, v[40:41]
	global_load_dwordx4 v[60:63], v[42:43], off
	global_load_dwordx4 v[56:59], v[40:41], off
	global_load_dwordx4 v[44:47], v[42:43], off offset:16
	s_nop 0
	global_load_dwordx4 v[40:43], v[40:41], off offset:16
	s_mul_i32 s16, s72, 0x90
	v_and_or_b32 v178, v178, 15, s16
	v_add_u32_e32 v180, s68, v178
	v_ashrrev_i32_e32 v181, 31, v180
	v_lshlrev_b64 v[180:181], 12, v[180:181]
	v_lshl_add_u64 v[198:199], s[50:51], 0, v[180:181]
	v_lshlrev_b64 v[176:177], 1, v[176:177]
	v_lshl_add_u64 v[198:199], v[198:199], 0, v[176:177]
	s_add_i32 s16, s68, 0x50
	s_and_b64 vcc, exec, s[30:31]
	s_mov_b32 s54, s42
	s_mov_b64 s[58:59], s[62:63]
	s_mov_b64 s[56:57], s[60:61]
	s_mov_b64 s[30:31], s[18:19]
	s_mov_b64 s[26:27], s[18:19]
	s_waitcnt vmcnt(3)
	v_add_f32_e32 v179, v214, v60
	s_waitcnt vmcnt(2)
	v_add_f32_e32 v181, v226, v56
	v_add_f32_e32 v183, v215, v61
	v_add_f32_e32 v197, v216, v62
	v_add_f32_e32 v201, v228, v58
	v_add_f32_e32 v203, v217, v63
	v_add_f32_e32 v195, v227, v57
	v_add_f32_e32 v204, v229, v59
	s_waitcnt vmcnt(1)
	v_add_f32_e32 v205, v222, v44
	v_add_f32_e32 v210, v223, v45
	v_add_f32_e32 v211, v224, v46
	s_waitcnt vmcnt(0)
; DI float sigmoidf_(float x) { return __builtin_amdgcn_rcpf(1.0f + __expf(-x)); }
	v_add_f32_e32 v212, v208, v42
	v_add_f32_e32 v213, v225, v47
	v_min_f32_e32 v180, 0x40e00000, v179
	v_med3_f32 v182, v181, s53, v194
	v_min_f32_e32 v181, 0x40e00000, v183
	v_min_f32_e32 v200, 0x40e00000, v197
	v_med3_f32 v202, v201, s53, v194
	v_min_f32_e32 v201, 0x40e00000, v203
	v_add_f32_e32 v214, v209, v43
	v_med3_f32 v183, v195, s53, v194
	v_med3_f32 v203, v204, s53, v194
	v_min_f32_e32 v204, 0x40e00000, v205
	v_min_f32_e32 v205, 0x40e00000, v210
	v_min_f32_e32 v208, 0x40e00000, v211
	v_med3_f32 v210, v212, s53, v194
	v_min_f32_e32 v209, 0x40e00000, v213
	v_med3_f32 v211, v214, s53, v194
	v_mul_f32_e32 v179, 0xc01d265f, v180
	v_mul_f32_e32 v195, 0xc01d265f, v181
	v_mul_f32_e32 v197, 0xc01d265f, v200
	v_mul_f32_e32 v212, 0xc01d265f, v201
	v_pk_fma_f32 v[200:201], v[202:203], v[200:201], v[200:201]
	v_pk_fma_f32 v[180:181], v[182:183], v[180:181], v[180:181]
	v_mul_f32_e32 v182, 0xc01d265f, v204
	v_mul_f32_e32 v183, 0xc01d265f, v205
	v_mul_f32_e32 v202, 0xc01d265f, v208
	v_mul_f32_e32 v203, 0xc01d265f, v209
	v_exp_f32_e32 v179, v179
	v_exp_f32_e32 v195, v195
	v_exp_f32_e32 v197, v197
	v_exp_f32_e32 v212, v212
	v_exp_f32_e32 v182, v182
	v_exp_f32_e32 v183, v183
	v_exp_f32_e32 v202, v202
	v_exp_f32_e32 v203, v203
	v_add_f32_e32 v179, 1.0, v179
	v_add_f32_e32 v195, 1.0, v195
	v_add_f32_e32 v197, 1.0, v197
	v_add_f32_e32 v212, 1.0, v212
	v_add_f32_e32 v213, 1.0, v182
	v_add_f32_e32 v214, 1.0, v183
	v_add_f32_e32 v215, 1.0, v202
	v_add_f32_e32 v216, 1.0, v203
	v_rcp_f32_e32 v182, v179
	v_rcp_f32_e32 v183, v195
	v_rcp_f32_e32 v202, v197
	v_rcp_f32_e32 v203, v212
	v_add_f32_e32 v206, v206, v40
	v_add_f32_e32 v207, v207, v41
	v_rcp_f32_e32 v212, v213
	v_rcp_f32_e32 v213, v214
	v_rcp_f32_e32 v214, v215
	v_rcp_f32_e32 v215, v216
	v_med3_f32 v206, v206, s53, v194
	v_med3_f32 v207, v207, s53, v194
	v_pk_mul_f32 v[182:183], v[180:181], v[182:183]
	v_pk_mul_f32 v[180:181], v[200:201], v[202:203]
	v_cvt_pk_bf16_f32 v181, v180, v181
	v_cvt_pk_bf16_f32 v180, v182, v183
	v_pk_fma_f32 v[200:201], v[206:207], v[204:205], v[204:205]
	v_pk_fma_f32 v[182:183], v[210:211], v[208:209], v[208:209]
	v_add_f32_e32 v172, v172, v60
	v_pk_mul_f32 v[200:201], v[200:201], v[212:213]
	v_pk_mul_f32 v[182:183], v[182:183], v[214:215]
	v_min_f32_e32 v172, 0x40e00000, v172
	v_add_f32_e32 v173, v173, v61
	v_cvt_pk_bf16_f32 v183, v182, v183
	v_cvt_pk_bf16_f32 v182, v200, v201
	v_min_f32_e32 v173, 0x40e00000, v173
	global_store_dwordx4 v[198:199], v[180:183], off
	v_mul_f32_e32 v179, 0xc01d265f, v172
	v_exp_f32_e32 v179, v179
	v_mul_f32_e32 v182, 0xc01d265f, v173
	v_exp_f32_e32 v183, v182
	v_add_f32_e32 v174, v174, v62
	v_add_f32_e32 v179, 1.0, v179
	v_min_f32_e32 v174, 0x40e00000, v174
	v_rcp_f32_e32 v182, v179
	v_add_f32_e32 v179, 1.0, v183
	v_mul_f32_e32 v183, 0xc01d265f, v174
	v_exp_f32_e32 v195, v183
	v_add_f32_e32 v175, v175, v63
	v_min_f32_e32 v175, 0x40e00000, v175
	v_rcp_f32_e32 v183, v179
	v_add_f32_e32 v179, 1.0, v195
	v_mul_f32_e32 v195, 0xc01d265f, v175
	v_exp_f32_e32 v195, v195
	v_rcp_f32_e32 v198, v179
	v_add_f32_e32 v168, v168, v56
	v_add_f32_e32 v169, v169, v57
	v_add_f32_e32 v179, 1.0, v195
	v_add_f32_e32 v170, v170, v58
	v_add_f32_e32 v171, v171, v59
	v_rcp_f32_e32 v199, v179
	v_med3_f32 v168, v168, s53, v194
	v_med3_f32 v169, v169, s53, v194
	v_med3_f32 v170, v170, s53, v194
	v_med3_f32 v171, v171, s53, v194
	v_pk_fma_f32 v[168:169], v[168:169], v[172:173], v[172:173]
	v_pk_fma_f32 v[170:171], v[170:171], v[174:175], v[174:175]
	v_add_f32_e32 v164, v164, v44
	v_pk_mul_f32 v[172:173], v[168:169], v[182:183]
	v_pk_mul_f32 v[168:169], v[170:171], v[198:199]
	v_min_f32_e32 v164, 0x40e00000, v164
	v_cvt_pk_bf16_f32 v169, v168, v169
	v_add_f32_e32 v166, v166, v46
	v_add_f32_e32 v167, v167, v47
	v_mul_f32_e32 v168, 0xc01d265f, v164
	v_add_f32_e32 v165, v165, v45
	v_min_f32_e32 v166, 0x40e00000, v166
	v_min_f32_e32 v167, 0x40e00000, v167
	v_exp_f32_e32 v170, v168
	v_cvt_pk_bf16_f32 v168, v172, v173
	v_min_f32_e32 v165, 0x40e00000, v165
	v_mul_f32_e32 v172, 0xc01d265f, v166
	v_mul_f32_e32 v173, 0xc01d265f, v167
	v_mul_f32_e32 v171, 0xc01d265f, v165
	v_exp_f32_e32 v172, v172
	v_exp_f32_e32 v173, v173
	v_exp_f32_e32 v171, v171
	v_add_f32_e32 v170, 1.0, v170
	v_add_f32_e32 v172, 1.0, v172
	v_add_f32_e32 v173, 1.0, v173
	v_add_f32_e32 v171, 1.0, v171
	v_add_f32_e32 v162, v162, v42
	v_rcp_f32_e32 v172, v172
	v_add_f32_e32 v163, v163, v43
	v_rcp_f32_e32 v173, v173
	v_add_f32_e32 v160, v160, v40
	v_rcp_f32_e32 v170, v170
	v_add_f32_e32 v161, v161, v41
	v_rcp_f32_e32 v171, v171
	v_med3_f32 v162, v162, s53, v194
	v_med3_f32 v163, v163, s53, v194
	v_med3_f32 v160, v160, s53, v194
	v_med3_f32 v161, v161, s53, v194
	v_pk_fma_f32 v[162:163], v[162:163], v[166:167], v[166:167]
	v_add_f32_e32 v156, v156, v60
	v_add_f32_e32 v157, v157, v61
	v_add_f32_e32 v158, v158, v62
	v_add_f32_e32 v159, v159, v63
	v_pk_fma_f32 v[160:161], v[160:161], v[164:165], v[164:165]
	v_pk_mul_f32 v[162:163], v[162:163], v[172:173]
	v_min_f32_e32 v156, 0x40e00000, v156
	v_min_f32_e32 v157, 0x40e00000, v157
	v_min_f32_e32 v158, 0x40e00000, v158
	v_min_f32_e32 v159, 0x40e00000, v159
	v_pk_mul_f32 v[160:161], v[160:161], v[170:171]
	v_cvt_pk_bf16_f32 v171, v162, v163
	v_mul_f32_e32 v162, 0xc01d265f, v156
	v_mul_f32_e32 v163, 0xc01d265f, v157
	v_mul_f32_e32 v164, 0xc01d265f, v158
	v_mul_f32_e32 v165, 0xc01d265f, v159
	v_exp_f32_e32 v162, v162
	v_exp_f32_e32 v163, v163
	v_exp_f32_e32 v164, v164
	v_exp_f32_e32 v165, v165
	v_add_f32_e32 v162, 1.0, v162
	v_add_f32_e32 v163, 1.0, v163
	v_add_f32_e32 v164, 1.0, v164
	v_add_f32_e32 v165, 1.0, v165
	v_add_f32_e32 v152, v152, v56
	v_rcp_f32_e32 v162, v162
; DI float sigmoidf_(float x) { return __builtin_amdgcn_rcpf(1.0f + __expf(-x)); }
	v_add_f32_e32 v153, v153, v57
	v_rcp_f32_e32 v163, v163
	v_add_f32_e32 v154, v154, v58
	v_rcp_f32_e32 v164, v164
	v_add_f32_e32 v155, v155, v59
	v_rcp_f32_e32 v165, v165
	v_med3_f32 v152, v152, s53, v194
	v_med3_f32 v153, v153, s53, v194
	v_med3_f32 v154, v154, s53, v194
	v_med3_f32 v155, v155, s53, v194
	v_pk_fma_f32 v[152:153], v[152:153], v[156:157], v[156:157]
	v_pk_fma_f32 v[154:155], v[154:155], v[158:159], v[158:159]
	v_add_f32_e32 v144, v144, v44
	v_pk_mul_f32 v[156:157], v[152:153], v[162:163]
	v_pk_mul_f32 v[152:153], v[154:155], v[164:165]
	v_min_f32_e32 v144, 0x40e00000, v144
	v_cvt_pk_bf16_f32 v153, v152, v153
	v_add_f32_e32 v146, v146, v46
	v_add_f32_e32 v147, v147, v47
	v_mul_f32_e32 v152, 0xc01d265f, v144
	v_add_f32_e32 v145, v145, v45
	v_min_f32_e32 v146, 0x40e00000, v146
	v_min_f32_e32 v147, 0x40e00000, v147
	v_exp_f32_e32 v154, v152
	v_cvt_pk_bf16_f32 v152, v156, v157
	v_min_f32_e32 v145, 0x40e00000, v145
	v_mul_f32_e32 v156, 0xc01d265f, v146
	v_mul_f32_e32 v157, 0xc01d265f, v147
	v_mul_f32_e32 v155, 0xc01d265f, v145
	v_exp_f32_e32 v156, v156
	v_exp_f32_e32 v157, v157
	v_exp_f32_e32 v155, v155
	v_add_f32_e32 v154, 1.0, v154
	v_add_f32_e32 v156, 1.0, v156
	v_add_f32_e32 v157, 1.0, v157
	v_add_f32_e32 v155, 1.0, v155
	v_add_f32_e32 v150, v150, v42
	v_rcp_f32_e32 v156, v156
	v_add_f32_e32 v151, v151, v43
	v_rcp_f32_e32 v157, v157
	v_add_f32_e32 v148, v148, v40
	v_rcp_f32_e32 v154, v154
	v_add_f32_e32 v149, v149, v41
	v_rcp_f32_e32 v155, v155
	v_med3_f32 v150, v150, s53, v194
	v_med3_f32 v151, v151, s53, v194
	v_med3_f32 v148, v148, s53, v194
	v_med3_f32 v149, v149, s53, v194
	v_pk_fma_f32 v[146:147], v[150:151], v[146:147], v[146:147]
	v_add_f32_e32 v140, v140, v60
	v_add_f32_e32 v141, v141, v61
	v_add_f32_e32 v142, v142, v62
	v_add_f32_e32 v143, v143, v63
	v_pk_fma_f32 v[144:145], v[148:149], v[144:145], v[144:145]
	v_pk_mul_f32 v[146:147], v[146:147], v[156:157]
	v_min_f32_e32 v140, 0x40e00000, v140
	v_min_f32_e32 v141, 0x40e00000, v141
	v_min_f32_e32 v142, 0x40e00000, v142
	v_min_f32_e32 v143, 0x40e00000, v143
	v_pk_mul_f32 v[144:145], v[144:145], v[154:155]
	v_cvt_pk_bf16_f32 v155, v146, v147
	v_mul_f32_e32 v146, 0xc01d265f, v140
	v_mul_f32_e32 v147, 0xc01d265f, v141
	v_mul_f32_e32 v148, 0xc01d265f, v142
	v_mul_f32_e32 v149, 0xc01d265f, v143
	v_exp_f32_e32 v146, v146
	v_exp_f32_e32 v147, v147
	v_exp_f32_e32 v148, v148
	v_exp_f32_e32 v149, v149
	v_add_f32_e32 v146, 1.0, v146
	v_add_f32_e32 v147, 1.0, v147
	v_add_f32_e32 v148, 1.0, v148
	v_add_f32_e32 v149, 1.0, v149
	v_add_f32_e32 v136, v136, v56
	v_rcp_f32_e32 v146, v146
	v_add_f32_e32 v137, v137, v57
	v_rcp_f32_e32 v147, v147
	v_add_f32_e32 v138, v138, v58
	v_rcp_f32_e32 v148, v148
	v_add_f32_e32 v139, v139, v59
	v_rcp_f32_e32 v149, v149
	v_med3_f32 v136, v136, s53, v194
	v_med3_f32 v137, v137, s53, v194
	v_med3_f32 v138, v138, s53, v194
	v_med3_f32 v139, v139, s53, v194
	v_pk_fma_f32 v[136:137], v[136:137], v[140:141], v[140:141]
	v_pk_fma_f32 v[138:139], v[138:139], v[142:143], v[142:143]
	v_add_f32_e32 v132, v132, v44
	v_pk_mul_f32 v[140:141], v[136:137], v[146:147]
	v_pk_mul_f32 v[136:137], v[138:139], v[148:149]
	v_min_f32_e32 v132, 0x40e00000, v132
	v_cvt_pk_bf16_f32 v137, v136, v137
	v_add_f32_e32 v134, v134, v46
	v_add_f32_e32 v135, v135, v47
	v_mul_f32_e32 v136, 0xc01d265f, v132
	v_add_f32_e32 v133, v133, v45
	v_min_f32_e32 v134, 0x40e00000, v134
	v_min_f32_e32 v135, 0x40e00000, v135
	v_exp_f32_e32 v138, v136
	v_cvt_pk_bf16_f32 v136, v140, v141
	v_min_f32_e32 v133, 0x40e00000, v133
	v_mul_f32_e32 v140, 0xc01d265f, v134
	v_mul_f32_e32 v141, 0xc01d265f, v135
	v_mul_f32_e32 v139, 0xc01d265f, v133
	v_exp_f32_e32 v140, v140
	v_exp_f32_e32 v141, v141
	v_exp_f32_e32 v139, v139
	v_add_f32_e32 v138, 1.0, v138
	v_add_f32_e32 v140, 1.0, v140
	v_add_f32_e32 v141, 1.0, v141
	v_add_f32_e32 v139, 1.0, v139
	v_add_f32_e32 v130, v130, v42
	v_rcp_f32_e32 v140, v140
	v_add_f32_e32 v131, v131, v43
	v_rcp_f32_e32 v141, v141
	v_add_f32_e32 v128, v128, v40
	v_rcp_f32_e32 v138, v138
	v_add_f32_e32 v129, v129, v41
	v_rcp_f32_e32 v139, v139
	v_med3_f32 v130, v130, s53, v194
	v_med3_f32 v131, v131, s53, v194
	v_med3_f32 v128, v128, s53, v194
	v_med3_f32 v129, v129, s53, v194
	v_pk_fma_f32 v[130:131], v[130:131], v[134:135], v[134:135]
	v_add_f32_e32 v124, v124, v60
	v_add_f32_e32 v125, v125, v61
	v_add_f32_e32 v126, v126, v62
	v_add_f32_e32 v127, v127, v63
	v_pk_fma_f32 v[128:129], v[128:129], v[132:133], v[132:133]
	v_pk_mul_f32 v[130:131], v[130:131], v[140:141]
	v_min_f32_e32 v124, 0x40e00000, v124
	v_min_f32_e32 v125, 0x40e00000, v125
	v_min_f32_e32 v126, 0x40e00000, v126
	v_min_f32_e32 v127, 0x40e00000, v127
	v_pk_mul_f32 v[128:129], v[128:129], v[138:139]
	v_cvt_pk_bf16_f32 v139, v130, v131
	v_mul_f32_e32 v130, 0xc01d265f, v124
	v_mul_f32_e32 v131, 0xc01d265f, v125
	v_mul_f32_e32 v132, 0xc01d265f, v126
	v_mul_f32_e32 v133, 0xc01d265f, v127
	v_exp_f32_e32 v130, v130
	v_exp_f32_e32 v131, v131
	v_exp_f32_e32 v132, v132
	v_exp_f32_e32 v133, v133
	v_add_f32_e32 v130, 1.0, v130
	v_add_f32_e32 v131, 1.0, v131
	v_add_f32_e32 v132, 1.0, v132
	v_add_f32_e32 v133, 1.0, v133
	v_add_f32_e32 v120, v120, v56
	v_rcp_f32_e32 v130, v130
	v_add_f32_e32 v121, v121, v57
	v_rcp_f32_e32 v131, v131
	v_add_f32_e32 v122, v122, v58
	v_rcp_f32_e32 v132, v132
	v_add_f32_e32 v123, v123, v59
	v_rcp_f32_e32 v133, v133
	v_med3_f32 v120, v120, s53, v194
	v_med3_f32 v121, v121, s53, v194
	v_med3_f32 v122, v122, s53, v194
	v_med3_f32 v123, v123, s53, v194
	v_pk_fma_f32 v[120:121], v[120:121], v[124:125], v[124:125]
	v_pk_fma_f32 v[122:123], v[122:123], v[126:127], v[126:127]
	v_add_f32_e32 v112, v112, v44
; DI float sigmoidf_(float x) { return __builtin_amdgcn_rcpf(1.0f + __expf(-x)); }
	v_pk_mul_f32 v[124:125], v[120:121], v[130:131]
	v_pk_mul_f32 v[120:121], v[122:123], v[132:133]
	v_min_f32_e32 v112, 0x40e00000, v112
	v_cvt_pk_bf16_f32 v121, v120, v121
	v_add_f32_e32 v114, v114, v46
	v_add_f32_e32 v115, v115, v47
	v_mul_f32_e32 v120, 0xc01d265f, v112
	v_add_f32_e32 v113, v113, v45
	v_min_f32_e32 v114, 0x40e00000, v114
	v_min_f32_e32 v115, 0x40e00000, v115
	v_exp_f32_e32 v122, v120
	v_cvt_pk_bf16_f32 v120, v124, v125
	v_min_f32_e32 v113, 0x40e00000, v113
	v_mul_f32_e32 v124, 0xc01d265f, v114
	v_mul_f32_e32 v125, 0xc01d265f, v115
	v_mul_f32_e32 v123, 0xc01d265f, v113
	v_exp_f32_e32 v124, v124
	v_exp_f32_e32 v125, v125
	v_exp_f32_e32 v123, v123
	v_add_f32_e32 v122, 1.0, v122
	v_add_f32_e32 v124, 1.0, v124
	v_add_f32_e32 v125, 1.0, v125
	v_add_f32_e32 v123, 1.0, v123
	v_add_f32_e32 v118, v118, v42
	v_rcp_f32_e32 v124, v124
	v_add_f32_e32 v119, v119, v43
	v_rcp_f32_e32 v125, v125
	v_add_f32_e32 v116, v116, v40
	v_rcp_f32_e32 v122, v122
	v_add_f32_e32 v117, v117, v41
	v_rcp_f32_e32 v123, v123
	v_med3_f32 v118, v118, s53, v194
	v_med3_f32 v119, v119, s53, v194
	v_med3_f32 v116, v116, s53, v194
	v_med3_f32 v117, v117, s53, v194
	v_pk_fma_f32 v[114:115], v[118:119], v[114:115], v[114:115]
	v_add_f32_e32 v108, v108, v60
	v_add_f32_e32 v109, v109, v61
	v_add_f32_e32 v110, v110, v62
	v_add_f32_e32 v111, v111, v63
	v_pk_fma_f32 v[112:113], v[116:117], v[112:113], v[112:113]
	v_pk_mul_f32 v[114:115], v[114:115], v[124:125]
	v_min_f32_e32 v108, 0x40e00000, v108
	v_min_f32_e32 v109, 0x40e00000, v109
	v_min_f32_e32 v110, 0x40e00000, v110
	v_min_f32_e32 v111, 0x40e00000, v111
	v_pk_mul_f32 v[112:113], v[112:113], v[122:123]
	v_cvt_pk_bf16_f32 v123, v114, v115
	v_mul_f32_e32 v114, 0xc01d265f, v108
	v_mul_f32_e32 v115, 0xc01d265f, v109
	v_mul_f32_e32 v116, 0xc01d265f, v110
	v_mul_f32_e32 v117, 0xc01d265f, v111
	v_exp_f32_e32 v114, v114
	v_exp_f32_e32 v115, v115
	v_exp_f32_e32 v116, v116
	v_exp_f32_e32 v117, v117
	v_add_f32_e32 v114, 1.0, v114
	v_add_f32_e32 v115, 1.0, v115
	v_add_f32_e32 v116, 1.0, v116
	v_add_f32_e32 v117, 1.0, v117
	v_add_f32_e32 v104, v104, v56
	v_rcp_f32_e32 v114, v114
	v_add_f32_e32 v105, v105, v57
	v_rcp_f32_e32 v115, v115
	v_add_f32_e32 v106, v106, v58
	v_rcp_f32_e32 v116, v116
	v_add_f32_e32 v107, v107, v59
	v_rcp_f32_e32 v117, v117
	v_med3_f32 v104, v104, s53, v194
	v_med3_f32 v105, v105, s53, v194
	v_med3_f32 v106, v106, s53, v194
	v_med3_f32 v107, v107, s53, v194
	v_pk_fma_f32 v[104:105], v[104:105], v[108:109], v[108:109]
	v_pk_fma_f32 v[106:107], v[106:107], v[110:111], v[110:111]
	v_add_f32_e32 v100, v100, v44
	v_pk_mul_f32 v[108:109], v[104:105], v[114:115]
	v_pk_mul_f32 v[104:105], v[106:107], v[116:117]
	v_min_f32_e32 v100, 0x40e00000, v100
	v_cvt_pk_bf16_f32 v105, v104, v105
	v_add_f32_e32 v102, v102, v46
	v_add_f32_e32 v103, v103, v47
	v_mul_f32_e32 v104, 0xc01d265f, v100
	v_add_f32_e32 v101, v101, v45
	v_min_f32_e32 v102, 0x40e00000, v102
	v_min_f32_e32 v103, 0x40e00000, v103
	v_exp_f32_e32 v106, v104
	v_cvt_pk_bf16_f32 v104, v108, v109
	v_min_f32_e32 v101, 0x40e00000, v101
	v_mul_f32_e32 v108, 0xc01d265f, v102
	v_mul_f32_e32 v109, 0xc01d265f, v103
	v_mul_f32_e32 v107, 0xc01d265f, v101
	v_exp_f32_e32 v108, v108
	v_exp_f32_e32 v109, v109
	v_exp_f32_e32 v107, v107
	v_add_f32_e32 v106, 1.0, v106
	v_add_f32_e32 v108, 1.0, v108
	v_add_f32_e32 v109, 1.0, v109
	v_add_f32_e32 v107, 1.0, v107
	v_add_f32_e32 v98, v98, v42
	v_rcp_f32_e32 v108, v108
	v_add_f32_e32 v99, v99, v43
	v_rcp_f32_e32 v109, v109
	v_add_f32_e32 v96, v96, v40
	v_rcp_f32_e32 v106, v106
	v_add_f32_e32 v97, v97, v41
	v_rcp_f32_e32 v107, v107
	v_med3_f32 v98, v98, s53, v194
	v_med3_f32 v99, v99, s53, v194
	v_med3_f32 v96, v96, s53, v194
	v_med3_f32 v97, v97, s53, v194
	v_pk_fma_f32 v[98:99], v[98:99], v[102:103], v[102:103]
	v_add_f32_e32 v92, v92, v60
	v_add_f32_e32 v93, v93, v61
	v_add_f32_e32 v94, v94, v62
	v_add_f32_e32 v95, v95, v63
	v_pk_fma_f32 v[96:97], v[96:97], v[100:101], v[100:101]
	v_pk_mul_f32 v[98:99], v[98:99], v[108:109]
	v_min_f32_e32 v92, 0x40e00000, v92
	v_min_f32_e32 v93, 0x40e00000, v93
	v_min_f32_e32 v94, 0x40e00000, v94
	v_min_f32_e32 v95, 0x40e00000, v95
	v_pk_mul_f32 v[96:97], v[96:97], v[106:107]
	v_cvt_pk_bf16_f32 v107, v98, v99
	v_mul_f32_e32 v98, 0xc01d265f, v92
	v_mul_f32_e32 v99, 0xc01d265f, v93
	v_mul_f32_e32 v100, 0xc01d265f, v94
	v_mul_f32_e32 v101, 0xc01d265f, v95
	v_exp_f32_e32 v98, v98
	v_exp_f32_e32 v99, v99
	v_exp_f32_e32 v100, v100
	v_exp_f32_e32 v101, v101
	v_add_f32_e32 v98, 1.0, v98
	v_add_f32_e32 v99, 1.0, v99
	v_add_f32_e32 v100, 1.0, v100
	v_add_f32_e32 v101, 1.0, v101
	v_add_f32_e32 v88, v88, v56
	v_rcp_f32_e32 v98, v98
	v_add_f32_e32 v89, v89, v57
	v_rcp_f32_e32 v99, v99
	v_add_f32_e32 v90, v90, v58
	v_rcp_f32_e32 v100, v100
	v_add_f32_e32 v91, v91, v59
	v_rcp_f32_e32 v101, v101
	v_med3_f32 v88, v88, s53, v194
	v_med3_f32 v89, v89, s53, v194
	v_med3_f32 v90, v90, s53, v194
	v_med3_f32 v91, v91, s53, v194
	v_pk_fma_f32 v[88:89], v[88:89], v[92:93], v[92:93]
	v_pk_fma_f32 v[90:91], v[90:91], v[94:95], v[94:95]
	v_add_f32_e32 v80, v80, v44
	v_pk_mul_f32 v[92:93], v[88:89], v[98:99]
	v_pk_mul_f32 v[88:89], v[90:91], v[100:101]
	v_min_f32_e32 v80, 0x40e00000, v80
	v_cvt_pk_bf16_f32 v89, v88, v89
	v_add_f32_e32 v82, v82, v46
	v_add_f32_e32 v83, v83, v47
	v_mul_f32_e32 v88, 0xc01d265f, v80
	v_add_f32_e32 v81, v81, v45
	v_min_f32_e32 v82, 0x40e00000, v82
	v_min_f32_e32 v83, 0x40e00000, v83
	v_exp_f32_e32 v90, v88
	v_cvt_pk_bf16_f32 v88, v92, v93
	v_min_f32_e32 v81, 0x40e00000, v81
	v_mul_f32_e32 v92, 0xc01d265f, v82
	v_mul_f32_e32 v93, 0xc01d265f, v83
	v_mul_f32_e32 v91, 0xc01d265f, v81
	v_exp_f32_e32 v92, v92
	v_exp_f32_e32 v93, v93
	v_exp_f32_e32 v91, v91
	v_add3_u32 v180, s68, 16, v178
	v_ashrrev_i32_e32 v181, 31, v180
	v_lshlrev_b64 v[180:181], 12, v[180:181]
	v_add_f32_e32 v92, 1.0, v92
	v_add_f32_e32 v93, 1.0, v93
	v_lshl_add_u64 v[180:181], s[50:51], 0, v[180:181]
	v_add_f32_e32 v90, 1.0, v90
	v_add_f32_e32 v91, 1.0, v91
	v_add_f32_e32 v86, v86, v42
	v_rcp_f32_e32 v92, v92
	v_add_f32_e32 v87, v87, v43
	v_rcp_f32_e32 v93, v93
	v_cvt_pk_bf16_f32 v170, v160, v161
	v_lshl_add_u64 v[160:161], v[180:181], 0, v[176:177]
	v_add_f32_e32 v84, v84, v40
	v_rcp_f32_e32 v90, v90
	v_add_f32_e32 v85, v85, v41
	v_rcp_f32_e32 v91, v91
	v_med3_f32 v86, v86, s53, v194
	v_med3_f32 v87, v87, s53, v194
	global_store_dwordx4 v[160:161], v[168:171], off
	v_add3_u32 v160, s68, 32, v178
	v_med3_f32 v84, v84, s53, v194
	v_med3_f32 v85, v85, s53, v194
	v_ashrrev_i32_e32 v161, 31, v160
	v_pk_fma_f32 v[82:83], v[86:87], v[82:83], v[82:83]
	v_add_f32_e32 v76, v76, v60
	v_add_f32_e32 v77, v77, v61
	v_add_f32_e32 v78, v78, v62
	v_add_f32_e32 v79, v79, v63
	v_lshlrev_b64 v[160:161], 12, v[160:161]
	v_pk_fma_f32 v[80:81], v[84:85], v[80:81], v[80:81]
	v_pk_mul_f32 v[82:83], v[82:83], v[92:93]
	v_min_f32_e32 v76, 0x40e00000, v76
	v_min_f32_e32 v77, 0x40e00000, v77
	v_min_f32_e32 v78, 0x40e00000, v78
	v_min_f32_e32 v79, 0x40e00000, v79
	v_add_f32_e32 v52, v52, v60
	v_add_f32_e32 v36, v36, v44
	v_lshl_add_u64 v[160:161], s[50:51], 0, v[160:161]
	v_pk_mul_f32 v[80:81], v[80:81], v[90:91]
	v_cvt_pk_bf16_f32 v91, v82, v83
	v_min_f32_e32 v52, 0x40e00000, v52
	v_min_f32_e32 v36, 0x40e00000, v36
	v_cvt_pk_bf16_f32 v154, v144, v145
	v_lshl_add_u64 v[144:145], v[160:161], 0, v[176:177]
	v_mul_f32_e32 v82, 0xc01d265f, v76
	v_mul_f32_e32 v83, 0xc01d265f, v77
	v_mul_f32_e32 v84, 0xc01d265f, v78
	v_mul_f32_e32 v85, 0xc01d265f, v79
	v_add_f32_e32 v68, v68, v44
	global_store_dwordx4 v[144:145], v[152:155], off
	v_add3_u32 v144, s68, 48, v178
	v_exp_f32_e32 v82, v82
	v_exp_f32_e32 v83, v83
	v_exp_f32_e32 v84, v84
	v_exp_f32_e32 v85, v85
	v_mul_f32_e32 v60, 0xc01d265f, v52
	v_mul_f32_e32 v44, 0xc01d265f, v36
	v_ashrrev_i32_e32 v145, 31, v144
	v_exp_f32_e32 v60, v60
	v_exp_f32_e32 v44, v44
	v_lshlrev_b64 v[144:145], 12, v[144:145]
	v_lshl_add_u64 v[144:145], s[50:51], 0, v[144:145]
	v_add_f32_e32 v53, v53, v61
	v_add_f32_e32 v37, v37, v45
	v_cvt_pk_bf16_f32 v138, v128, v129
	v_lshl_add_u64 v[128:129], v[144:145], 0, v[176:177]
	v_add_f32_e32 v82, 1.0, v82
	v_add_f32_e32 v83, 1.0, v83
	v_add_f32_e32 v84, 1.0, v84
	v_add_f32_e32 v85, 1.0, v85
	v_min_f32_e32 v53, 0x40e00000, v53
	v_min_f32_e32 v37, 0x40e00000, v37
	global_store_dwordx4 v[128:129], v[136:139], off
	v_add3_u32 v128, s68, 64, v178
	v_add_f32_e32 v72, v72, v56
	v_rcp_f32_e32 v82, v82
	v_add_f32_e32 v73, v73, v57
	v_rcp_f32_e32 v83, v83
	v_add_f32_e32 v74, v74, v58
	v_rcp_f32_e32 v84, v84
	v_add_f32_e32 v75, v75, v59
	v_rcp_f32_e32 v85, v85
	v_add_f32_e32 v64, v64, v40
	v_add_f32_e32 v48, v48, v56
	v_add_f32_e32 v56, 1.0, v60
	v_add_f32_e32 v32, v32, v40
	v_add_f32_e32 v40, 1.0, v44
	v_ashrrev_i32_e32 v129, 31, v128
	v_med3_f32 v72, v72, s53, v194
	v_med3_f32 v73, v73, s53, v194
	v_med3_f32 v74, v74, s53, v194
	v_med3_f32 v75, v75, s53, v194
	v_mul_f32_e32 v60, 0xc01d265f, v53
	v_mul_f32_e32 v44, 0xc01d265f, v37
	v_lshlrev_b64 v[128:129], 12, v[128:129]
	v_exp_f32_e32 v60, v60
	v_exp_f32_e32 v44, v44
	v_lshl_add_u64 v[128:129], s[50:51], 0, v[128:129]
	v_pk_fma_f32 v[74:75], v[74:75], v[78:79], v[78:79]
	v_pk_fma_f32 v[72:73], v[72:73], v[76:77], v[76:77]
	v_cvt_pk_bf16_f32 v122, v112, v113
	v_lshl_add_u64 v[112:113], v[128:129], 0, v[176:177]
	v_pk_mul_f32 v[76:77], v[72:73], v[82:83]
	v_pk_mul_f32 v[72:73], v[74:75], v[84:85]
	v_min_f32_e32 v68, 0x40e00000, v68
	v_add_f32_e32 v54, v54, v62
	v_add_f32_e32 v38, v38, v46
	global_store_dwordx4 v[112:113], v[120:123], off
	v_add_u32_e32 v112, s16, v178
	v_cvt_pk_bf16_f32 v73, v72, v73
	v_add_f32_e32 v69, v69, v45
	v_add_f32_e32 v70, v70, v46
	v_add_f32_e32 v71, v71, v47
; DI int lane_id() { int l; asm volatile("v_mbcnt_lo_u32_b32 %0, -1, 0\n\tv_mbcnt_hi_u32_b32 %0, -1, %0" : "=v"(l)); return l; }
;     ...
;         { const int l2 = lane_id(); cur.ep(acc, wr, wc, l2 & 15, l2 >> 4); }
;         if (!has_next) break;
	v_min_f32_e32 v54, 0x40e00000, v54
	v_min_f32_e32 v38, 0x40e00000, v38
	v_ashrrev_i32_e32 v113, 31, v112
	v_mul_f32_e32 v72, 0xc01d265f, v68
	v_min_f32_e32 v69, 0x40e00000, v69
	v_add_f32_e32 v65, v65, v41
	v_min_f32_e32 v70, 0x40e00000, v70
	v_min_f32_e32 v71, 0x40e00000, v71
	v_add_f32_e32 v49, v49, v57
	v_add_f32_e32 v57, 1.0, v60
	v_add_f32_e32 v33, v33, v41
	v_add_f32_e32 v41, 1.0, v44
	v_lshlrev_b64 v[112:113], 12, v[112:113]
	v_exp_f32_e32 v74, v72
	v_cvt_pk_bf16_f32 v72, v76, v77
	v_mul_f32_e32 v60, 0xc01d265f, v54
	v_mul_f32_e32 v44, 0xc01d265f, v38
	v_lshl_add_u64 v[112:113], s[50:51], 0, v[112:113]
	v_mul_f32_e32 v75, 0xc01d265f, v69
	v_mul_f32_e32 v76, 0xc01d265f, v70
	v_mul_f32_e32 v77, 0xc01d265f, v71
	v_exp_f32_e32 v60, v60
	v_exp_f32_e32 v44, v44
	v_cvt_pk_bf16_f32 v106, v96, v97
	v_lshl_add_u64 v[96:97], v[112:113], 0, v[176:177]
	s_add_i32 s16, s68, 0x60
	v_exp_f32_e32 v75, v75
	v_exp_f32_e32 v76, v76
	v_exp_f32_e32 v77, v77
	global_store_dwordx4 v[96:97], v[104:107], off
	v_add_u32_e32 v96, s16, v178
	v_add_f32_e32 v55, v55, v63
	v_add_f32_e32 v39, v39, v47
	v_ashrrev_i32_e32 v97, 31, v96
	v_min_f32_e32 v55, 0x40e00000, v55
	v_min_f32_e32 v39, 0x40e00000, v39
	v_lshlrev_b64 v[96:97], 12, v[96:97]
	v_add_f32_e32 v66, v66, v42
	v_add_f32_e32 v50, v50, v58
	v_add_f32_e32 v58, 1.0, v60
	v_add_f32_e32 v34, v34, v42
	v_add_f32_e32 v42, 1.0, v44
	v_lshl_add_u64 v[96:97], s[50:51], 0, v[96:97]
	v_add_f32_e32 v74, 1.0, v74
	v_add_f32_e32 v75, 1.0, v75
	v_add_f32_e32 v76, 1.0, v76
	v_add_f32_e32 v77, 1.0, v77
	v_mul_f32_e32 v60, 0xc01d265f, v55
	v_mul_f32_e32 v44, 0xc01d265f, v39
	v_cvt_pk_bf16_f32 v90, v80, v81
	v_lshl_add_u64 v[80:81], v[96:97], 0, v[176:177]
	s_add_i32 s16, s68, 0x70
	v_rcp_f32_e32 v74, v74
	v_rcp_f32_e32 v75, v75
	v_rcp_f32_e32 v76, v76
	v_add_f32_e32 v67, v67, v43
	v_rcp_f32_e32 v77, v77
	v_exp_f32_e32 v60, v60
	v_exp_f32_e32 v44, v44
	global_store_dwordx4 v[80:81], v[88:91], off
	v_add_u32_e32 v80, s16, v178
	v_med3_f32 v64, v64, s53, v194
	v_med3_f32 v65, v65, s53, v194
	v_med3_f32 v66, v66, s53, v194
	v_med3_f32 v67, v67, s53, v194
	v_ashrrev_i32_e32 v81, 31, v80
	v_lshlrev_b64 v[80:81], 12, v[80:81]
	v_pk_fma_f32 v[66:67], v[66:67], v[70:71], v[70:71]
	v_pk_fma_f32 v[64:65], v[64:65], v[68:69], v[68:69]
	v_lshl_add_u64 v[80:81], s[50:51], 0, v[80:81]
	v_pk_mul_f32 v[64:65], v[64:65], v[74:75]
	v_pk_mul_f32 v[66:67], v[66:67], v[76:77]
	v_add_f32_e32 v51, v51, v59
	v_add_f32_e32 v59, 1.0, v60
	v_add_f32_e32 v35, v35, v43
	v_add_f32_e32 v43, 1.0, v44
	v_cvt_pk_bf16_f32 v75, v66, v67
	v_cvt_pk_bf16_f32 v74, v64, v65
	v_lshl_add_u64 v[64:65], v[80:81], 0, v[176:177]
	s_add_i32 s16, s68, 0x80
	v_rcp_f32_e32 v56, v56
	v_rcp_f32_e32 v57, v57
	v_rcp_f32_e32 v58, v58
	v_rcp_f32_e32 v59, v59
	v_rcp_f32_e32 v40, v40
	v_rcp_f32_e32 v41, v41
	v_rcp_f32_e32 v42, v42
	v_rcp_f32_e32 v43, v43
	global_store_dwordx4 v[64:65], v[72:75], off
	v_add_u32_e32 v64, s16, v178
	v_med3_f32 v48, v48, s53, v194
	v_med3_f32 v49, v49, s53, v194
	v_med3_f32 v50, v50, s53, v194
	v_med3_f32 v51, v51, s53, v194
	v_med3_f32 v32, v32, s53, v194
	v_med3_f32 v33, v33, s53, v194
	v_med3_f32 v34, v34, s53, v194
	v_med3_f32 v35, v35, s53, v194
	v_ashrrev_i32_e32 v65, 31, v64
	v_lshlrev_b64 v[64:65], 12, v[64:65]
	v_pk_fma_f32 v[50:51], v[50:51], v[54:55], v[54:55]
	v_pk_fma_f32 v[48:49], v[48:49], v[52:53], v[52:53]
	v_pk_fma_f32 v[34:35], v[34:35], v[38:39], v[38:39]
	v_pk_fma_f32 v[32:33], v[32:33], v[36:37], v[36:37]
	v_lshl_add_u64 v[64:65], s[50:51], 0, v[64:65]
	v_pk_mul_f32 v[52:53], v[48:49], v[56:57]
	v_pk_mul_f32 v[48:49], v[50:51], v[58:59]
	v_pk_mul_f32 v[32:33], v[32:33], v[40:41]
	v_pk_mul_f32 v[34:35], v[34:35], v[42:43]
	v_cvt_pk_bf16_f32 v49, v48, v49
	v_cvt_pk_bf16_f32 v48, v52, v53
	v_cvt_pk_bf16_f32 v51, v34, v35
	v_cvt_pk_bf16_f32 v50, v32, v33
	v_lshl_add_u64 v[32:33], v[64:65], 0, v[176:177]
	s_mov_b32 s68, s43
	global_store_dwordx4 v[32:33], v[48:51], off
	s_cbranch_vccnz .LBB0_663
